# prep: code/kernarg touch loads moved to the very end of each wave (off the load->reduce->barrier path), 72 VGPRs; stream as v23
# speedup vs baseline: 1.0098x; 1.0098x over previous
.Lprep_ld_done:
	s_getpc_b64 s[22:23]
	s_and_b32 s22, s22, 0xffffff00
	v_lshlrev_b32_e32 v25, 4, v0
	v_subrev_u32_e32 v30, 0x280, v0
	s_waitcnt vmcnt(0)
	v_pk_mul_f32 v[12:13], v[12:13], v[16:17] op_sel_hi:[1,0]
	v_pk_mul_f32 v[14:15], v[14:15], v[16:17] op_sel_hi:[1,0]
	v_pk_fma_f32 v[8:9], v[8:9], v[6:7], v[12:13] op_sel_hi:[1,0,1]
	v_pk_fma_f32 v[10:11], v[10:11], v[6:7], v[14:15] op_sel_hi:[1,0,1]
	s_nop 1
	v_add_f32_dpp v8, v8, v8 row_ror:8 row_mask:0xf bank_mask:0xf bound_ctrl:1
	v_add_f32_dpp v9, v9, v9 row_ror:8 row_mask:0xf bank_mask:0xf bound_ctrl:1
	v_add_f32_dpp v10, v10, v10 row_ror:8 row_mask:0xf bank_mask:0xf bound_ctrl:1
	v_add_f32_dpp v11, v11, v11 row_ror:8 row_mask:0xf bank_mask:0xf bound_ctrl:1
	v_mov_b32_e32 v12, v8
	v_mov_b32_e32 v13, v9
	v_mov_b32_e32 v14, v10
	v_mov_b32_e32 v15, v11
	v_permlane16_swap_b32_e32 v8, v12
	v_permlane16_swap_b32_e32 v9, v13
	v_permlane16_swap_b32_e32 v10, v14
	v_permlane16_swap_b32_e32 v11, v15
	v_add_f32_e32 v8, v8, v12
	v_add_f32_e32 v9, v9, v13
	v_add_f32_e32 v10, v10, v14
	v_add_f32_e32 v11, v11, v15
	v_mov_b32_e32 v12, v8
	v_mov_b32_e32 v13, v9
	v_mov_b32_e32 v14, v10
	v_mov_b32_e32 v15, v11
	v_permlane32_swap_b32_e32 v8, v12
	v_permlane32_swap_b32_e32 v9, v13
	v_permlane32_swap_b32_e32 v10, v14
	v_permlane32_swap_b32_e32 v11, v15
	v_add_f32_e32 v8, v8, v12
	v_add_f32_e32 v9, v9, v13
	v_add_f32_e32 v10, v10, v14
	v_add_f32_e32 v11, v11, v15
	v_lshlrev_b32_e32 v21, 4, v19
	v_lshl_add_u32 v21, v20, 7, v21
	v_cmp_gt_u32_e32 vcc, 8, v19
	s_and_saveexec_b64 s[20:21], vcc
	ds_write_b128 v21, v[8:11]
	s_mov_b64 exec, s[20:21]
	s_cmp_lg_u32 s2, 0
	s_cbranch_scc1 .Lprep_bar
	v_mul_f32_e32 v23, v23, v24
	s_nop 1
	v_add_f32_dpp v23, v23, v23 quad_perm:[1,0,3,2] row_mask:0xf bank_mask:0xf bound_ctrl:1
	s_nop 1
	v_add_f32_dpp v23, v23, v23 quad_perm:[2,3,0,1] row_mask:0xf bank_mask:0xf bound_ctrl:1
	s_nop 1
	v_add_f32_dpp v23, v23, v23 row_ror:4 row_mask:0xf bank_mask:0xf bound_ctrl:1
	s_nop 1
	v_add_f32_dpp v23, v23, v23 row_ror:8 row_mask:0xf bank_mask:0xf bound_ctrl:1
	v_mov_b32_e32 v24, v23
	s_nop 1
	v_permlane16_swap_b32_e32 v23, v24
	v_add_f32_e32 v23, v23, v24
	v_mov_b32_e32 v24, v23
	s_nop 1
	v_permlane32_swap_b32_e32 v23, v24
	v_add_f32_e32 v23, v23, v24
	v_lshlrev_b32_e32 v22, 2, v20
	v_cmp_eq_u32_e32 vcc, 0, v19
	s_and_saveexec_b64 s[20:21], vcc
	ds_write_b32 v22, v23 offset:2048
	s_mov_b64 exec, s[20:21]
.Lprep_bar:
	s_waitcnt lgkmcnt(0)
	s_barrier
	s_cmp_lt_u32 s14, 32
	s_cbranch_scc1 .Lprep_hid
	v_cmp_gt_u32_e32 vcc, 32, v0
	s_and_saveexec_b64 s[20:21], vcc
	s_cbranch_execz .Lprep_done
	v_lshlrev_b32_e32 v1, 2, v0
	ds_read2_b32 v[2:3], v1 offset1:32
	ds_read2_b32 v[4:5], v1 offset0:64 offset1:96
	ds_read2_b32 v[6:7], v1 offset0:128 offset1:160
	ds_read2_b32 v[8:9], v1 offset0:192 offset1:224
	v_add_u32_e32 v10, 0x400, v1
	ds_read2_b32 v[12:13], v10 offset1:32
	ds_read2_b32 v[14:15], v10 offset0:64 offset1:96
	ds_read2_b32 v[16:17], v10 offset0:128 offset1:160
	ds_read2_b32 v[18:19], v10 offset0:192 offset1:224
	s_lshl_b32 s16, s15, 12
	s_add_i32 s16, s16, s17
	s_sub_i32 s16, s16, 0x1000
	v_add_u32_e32 v1, s16, v1
	s_waitcnt lgkmcnt(6)
	v_pk_add_f32 v[2:3], v[2:3], v[4:5]
	s_waitcnt lgkmcnt(4)
	v_pk_add_f32 v[6:7], v[6:7], v[8:9]
	s_waitcnt lgkmcnt(2)
	v_pk_add_f32 v[12:13], v[12:13], v[14:15]
	s_waitcnt lgkmcnt(0)
	v_pk_add_f32 v[16:17], v[16:17], v[18:19]
	v_pk_add_f32 v[2:3], v[2:3], v[6:7]
	v_pk_add_f32 v[12:13], v[12:13], v[16:17]
	s_nop 0
	v_pk_add_f32 v[2:3], v[2:3], v[12:13]
	s_nop 0
	v_add_f32_e32 v6, v2, v3
	global_store_dword v1, v6, s[12:13]
	s_branch .Lprep_done
.Lprep_hid:
	v_cmp_gt_u32_e32 vcc, 0x200, v0
	s_and_saveexec_b64 s[20:21], vcc
	s_cbranch_execz .Lprep_done
	v_and_b32_e32 v37, 31, v0
	v_lshlrev_b32_e32 v1, 2, v37
	ds_read2_b32 v[2:3], v1 offset1:32
	ds_read2_b32 v[4:5], v1 offset0:64 offset1:96
	ds_read2_b32 v[6:7], v1 offset0:128 offset1:160
	ds_read2_b32 v[8:9], v1 offset0:192 offset1:224
	v_add_u32_e32 v10, 0x400, v1
	ds_read2_b32 v[12:13], v10 offset1:32
	ds_read2_b32 v[14:15], v10 offset0:64 offset1:96
	ds_read2_b32 v[16:17], v10 offset0:128 offset1:160
	ds_read2_b32 v[18:19], v10 offset0:192 offset1:224
	s_waitcnt lgkmcnt(6)
	v_pk_add_f32 v[2:3], v[2:3], v[4:5]
	s_waitcnt lgkmcnt(4)
	v_pk_add_f32 v[6:7], v[6:7], v[8:9]
	s_waitcnt lgkmcnt(2)
	v_pk_add_f32 v[12:13], v[12:13], v[14:15]
	s_waitcnt lgkmcnt(0)
	v_pk_add_f32 v[16:17], v[16:17], v[18:19]
	v_pk_add_f32 v[2:3], v[2:3], v[6:7]
	v_pk_add_f32 v[12:13], v[12:13], v[16:17]
	s_nop 0
	v_pk_add_f32 v[2:3], v[2:3], v[12:13]
	s_nop 0
	v_add_f32_e32 v6, v2, v3
	v_mul_f32_e32 v6, v36, v6
	s_nop 1
	v_add_f32_dpp v6, v6, v6 quad_perm:[1,0,3,2] row_mask:0xf bank_mask:0xf bound_ctrl:1
	s_nop 1
	v_add_f32_dpp v6, v6, v6 quad_perm:[2,3,0,1] row_mask:0xf bank_mask:0xf bound_ctrl:1
	s_nop 1
	v_add_f32_dpp v6, v6, v6 row_ror:4 row_mask:0xf bank_mask:0xf bound_ctrl:1
	s_nop 1
	v_add_f32_dpp v6, v6, v6 row_ror:8 row_mask:0xf bank_mask:0xf bound_ctrl:1
	v_mov_b32_e32 v7, v6
	s_nop 1
	v_permlane16_swap_b32_e32 v6, v7
	v_add_f32_e32 v6, v6, v7
	v_lshrrev_b32_e32 v2, 5, v0
	v_lshlrev_b32_e32 v2, 2, v2
	s_lshl_b32 s16, s15, 11
	s_lshl_b32 s18, s14, 6
	s_add_i32 s16, s16, s18
	s_addk_i32 s16, 0x4000
	v_add_u32_e32 v2, s16, v2
	v_cmp_eq_u32_e32 vcc, 0, v37
	s_and_saveexec_b64 s[26:27], vcc
	global_store_dword v2, v6, s[12:13]
	s_mov_b64 exec, s[26:27]
	s_cmp_lg_u32 s2, 0
	s_cbranch_scc1 .Lprep_done
	v_cmp_eq_u32_e32 vcc, 0, v0
	s_and_saveexec_b64 s[26:27], vcc
	s_cbranch_execz .Lprep_done
	v_mov_b32_e32 v1, 0x800
	ds_read_b128 v[2:5], v1
	ds_read_b128 v[6:9], v1 offset:16
	ds_read_b128 v[10:13], v1 offset:32
	ds_read_b128 v[14:17], v1 offset:48
	v_mov_b32_e32 v1, 0x6000
	s_waitcnt lgkmcnt(0)
	v_pk_add_f32 v[2:3], v[2:3], v[4:5]
	v_pk_add_f32 v[6:7], v[6:7], v[8:9]
	v_pk_add_f32 v[10:11], v[10:11], v[12:13]
	v_pk_add_f32 v[14:15], v[14:15], v[16:17]
	v_pk_add_f32 v[2:3], v[2:3], v[6:7]
	v_pk_add_f32 v[10:11], v[10:11], v[14:15]
	s_nop 0
	v_pk_add_f32 v[2:3], v[2:3], v[10:11]
	s_nop 0
	v_add_f32_e32 v2, v2, v3
	global_store_dword v1, v2, s[12:13]
.Lprep_done:
	s_mov_b64 exec, -1
	s_movk_i32 s24, 0x240
	v_cmp_gt_u32_e32 vcc, s24, v0
	s_and_saveexec_b64 s[20:21], vcc
	s_cbranch_execz .Lprep_pf1
	global_load_dwordx4 v[26:29], v25, s[22:23]

.Lprep_pf2:
	s_mov_b64 exec, s[20:21]
.Lprep_exit:
	s_endpgm

	.amdhsa_kernel _Z11prep_kernelPKfS0_S0_S0_Pf
		.amdhsa_group_segment_fixed_size 2112
		.amdhsa_private_segment_fixed_size 0
		.amdhsa_kernarg_size 40
		.amdhsa_user_sgpr_count 2
		.amdhsa_user_sgpr_dispatch_ptr 0
		.amdhsa_user_sgpr_queue_ptr 0
		.amdhsa_user_sgpr_kernarg_segment_ptr 1
		.amdhsa_user_sgpr_dispatch_id 0
		.amdhsa_user_sgpr_kernarg_preload_length 0
		.amdhsa_user_sgpr_kernarg_preload_offset 0
		.amdhsa_user_sgpr_private_segment_size 0
		.amdhsa_uses_dynamic_stack 0
		.amdhsa_enable_private_segment 0
		.amdhsa_system_sgpr_workgroup_id_x 1
		.amdhsa_system_sgpr_workgroup_id_y 0
		.amdhsa_system_sgpr_workgroup_id_z 0
		.amdhsa_system_sgpr_workgroup_info 0
		.amdhsa_system_vgpr_workitem_id 0
		.amdhsa_next_free_vgpr 72
		.amdhsa_next_free_sgpr 28
		.amdhsa_accum_offset 72
		.amdhsa_reserve_vcc 1
		.amdhsa_float_round_mode_32 0
		.amdhsa_float_round_mode_16_64 0
		.amdhsa_float_denorm_mode_32 3
		.amdhsa_float_denorm_mode_16_64 3
		.amdhsa_dx10_clamp 1
		.amdhsa_ieee_mode 1
		.amdhsa_fp16_overflow 0
		.amdhsa_tg_split 0
		.amdhsa_exception_fp_ieee_invalid_op 0
		.amdhsa_exception_fp_denorm_src 0
		.amdhsa_exception_fp_ieee_div_zero 0
		.amdhsa_exception_fp_ieee_overflow 0
		.amdhsa_exception_fp_ieee_underflow 0
		.amdhsa_exception_fp_ieee_inexact 0
		.amdhsa_exception_int_div_zero 0
	.end_amdhsa_kernel

.Lfunc_end0:
	.size	_Z11prep_kernelPKfS0_S0_S0_Pf, .Lfunc_end0-_Z11prep_kernelPKfS0_S0_S0_Pf
	.set _Z11prep_kernelPKfS0_S0_S0_Pf.num_vgpr, 72
	.set _Z11prep_kernelPKfS0_S0_S0_Pf.num_agpr, 0
	.set _Z11prep_kernelPKfS0_S0_S0_Pf.numbered_sgpr, 28
	.set _Z11prep_kernelPKfS0_S0_S0_Pf.num_named_barrier, 0
	.set _Z11prep_kernelPKfS0_S0_S0_Pf.private_seg_size, 0
	.set _Z11prep_kernelPKfS0_S0_S0_Pf.uses_vcc, 1
	.set _Z11prep_kernelPKfS0_S0_S0_Pf.uses_flat_scratch, 0
	.set _Z11prep_kernelPKfS0_S0_S0_Pf.has_dyn_sized_stack, 0
	.set _Z11prep_kernelPKfS0_S0_S0_Pf.has_recursion, 0
	.set _Z11prep_kernelPKfS0_S0_S0_Pf.has_indirect_call, 0

amdhsa.kernels:
  - .agpr_count:     0
    .args:
      - .actual_access:  read_only
        .address_space:  global
        .offset:         0
        .size:           8
        .value_kind:     global_buffer
      - .actual_access:  read_only
        .address_space:  global
        .offset:         8
        .size:           8
        .value_kind:     global_buffer
      - .actual_access:  read_only
        .address_space:  global
        .offset:         16
        .size:           8
        .value_kind:     global_buffer
      - .actual_access:  read_only
        .address_space:  global
        .offset:         24
        .size:           8
        .value_kind:     global_buffer
      - .actual_access:  write_only
        .address_space:  global
        .offset:         32
        .size:           8
        .value_kind:     global_buffer
    .group_segment_fixed_size: 2112
    .kernarg_segment_align: 8
    .kernarg_segment_size: 40
    .language:       OpenCL C
    .language_version:
      - 2
      - 0
    .max_flat_workgroup_size: 1024
    .name:           _Z11prep_kernelPKfS0_S0_S0_Pf
    .private_segment_fixed_size: 0
    .sgpr_count:     34
    .sgpr_spill_count: 0
    .symbol:         _Z11prep_kernelPKfS0_S0_S0_Pf.kd
    .uniform_work_group_size: 1
    .uses_dynamic_stack: false
    .vgpr_count:     72
    .vgpr_spill_count: 0
    .wavefront_size: 64
  - .agpr_count:     0
    .args:
      - .actual_access:  read_only
        .address_space:  global
        .offset:         0
        .size:           8
        .value_kind:     global_buffer
      - .address_space:  global
        .offset:         8
        .size:           8
        .value_kind:     global_buffer
    .group_segment_fixed_size: 4096
    .kernarg_segment_align: 8
    .kernarg_segment_size: 16
    .language:       OpenCL C
    .language_version:
      - 2
      - 0
    .max_flat_workgroup_size: 1024
    .name:           _Z13stream_kernelPKfPf
    .private_segment_fixed_size: 0
    .sgpr_count:     17
    .sgpr_spill_count: 0
    .symbol:         _Z13stream_kernelPKfPf.kd
    .uniform_work_group_size: 1
    .uses_dynamic_stack: false
    .vgpr_count:     67
    .vgpr_spill_count: 0
    .wavefront_size: 64
  - .agpr_count:     0
    .args:
      - .actual_access:  read_only
        .address_space:  global
        .offset:         0
        .size:           8
        .value_kind:     global_buffer
      - .actual_access:  write_only
        .address_space:  global
        .offset:         8
        .size:           8
        .value_kind:     global_buffer
    .group_segment_fixed_size: 32
    .kernarg_segment_align: 8
    .kernarg_segment_size: 16
    .language:       OpenCL C
    .language_version:
      - 2
      - 0
    .max_flat_workgroup_size: 256
    .name:           _Z14softmax_kernelPKfPf
    .private_segment_fixed_size: 0
    .sgpr_count:     16
    .sgpr_spill_count: 0
    .symbol:         _Z14softmax_kernelPKfPf.kd
    .uniform_work_group_size: 1
    .uses_dynamic_stack: false
    .vgpr_count:     17
    .vgpr_spill_count: 0
    .wavefront_size: 64
